# row phases (norm1, norm2): nt on the residual-stream row loads and the expert-output gathers
# speedup vs baseline: 1.0084x; 1.0027x over previous
.LBB0_126:
	v_lshlrev_b32_e32 v50, 2, v124
	v_lshlrev_b64 v[18:19], 12, v[18:19]
	v_lshl_add_u64 v[18:19], v[20:21], 0, v[18:19]
	v_lshlrev_b32_e32 v130, 2, v50
	v_lshl_add_u64 v[18:19], v[18:19], 0, v[130:131]
	global_load_dwordx4 v[30:33], v[18:19], off nt
	global_load_dwordx4 v[26:29], v[18:19], off offset:1024 nt
	global_load_dwordx4 v[22:25], v[18:19], off offset:2048 nt
	s_nop 0
	global_load_dwordx4 v[18:21], v[18:19], off offset:3072 nt
	v_or_b32_e32 v34, 1, v126
	s_and_b64 vcc, exec, s[0:1]
	s_mov_b64 s[0:1], -1
	s_cbranch_vccnz .LBB0_128
	v_ashrrev_i32_e32 v35, 31, v34
	s_mov_b64 s[0:1], 0

.LBB0_134:
	v_lshlrev_b64 v[34:35], 12, v[34:35]
	v_lshl_add_u64 v[34:35], v[36:37], 0, v[34:35]
	v_lshl_add_u64 v[46:47], v[34:35], 0, v[130:131]
	global_load_dwordx4 v[34:37], v[46:47], off nt
	global_load_dwordx4 v[38:41], v[46:47], off offset:1024 nt
	global_load_dwordx4 v[42:45], v[46:47], off offset:2048 nt
	s_nop 0
	global_load_dwordx4 v[46:49], v[46:47], off offset:3072 nt
	v_cmp_gt_u32_e64 s[4:5], 16, v124
	s_and_b64 s[0:1], s[14:15], s[4:5]
	s_xor_b64 s[0:1], s[0:1], -1
	v_mov_b32_e32 v125, v131
	s_and_saveexec_b64 s[6:7], s[0:1]
	s_xor_b64 s[0:1], exec, s[6:7]
	s_or_saveexec_b64 s[0:1], s[0:1]
	v_mov_b32_e32 v170, 2.0
	v_mov_b32_e32 v171, 0
	s_xor_b64 exec, exec, s[0:1]
	s_cbranch_execz .LBB0_136
	v_lshlrev_b64 v[52:53], 2, v[124:125]
	v_lshlrev_b64 v[54:55], 6, v[126:127]
	v_or_b32_e32 v53, v55, v53
	v_or_b32_e32 v52, v54, v52
	v_lshl_add_u64 v[54:55], s[86:87], 0, v[52:53]
	v_lshl_add_u64 v[52:53], s[96:97], 0, v[52:53]
	global_load_dword v170, v[54:55], off
	global_load_dword v171, v[52:53], off

.LBB0_147:
	v_ashrrev_i32_e32 v99, 31, v98
	v_lshlrev_b64 v[98:99], 12, v[98:99]
	v_lshl_add_u64 v[98:99], v[100:101], 0, v[98:99]
	v_lshl_add_u64 v[110:111], v[98:99], 0, v[130:131]
	global_load_dwordx4 v[98:101], v[110:111], off nt
	global_load_dwordx4 v[102:105], v[110:111], off offset:1024 nt
	global_load_dwordx4 v[106:109], v[110:111], off offset:2048 nt
	s_nop 0
	global_load_dwordx4 v[110:113], v[110:111], off offset:3072 nt

.LBB0_157:
	s_add_u32 s50, s46, -1
	s_addc_u32 s51, s47, -1
	s_and_b64 vcc, s[50:51], s[46:47]
	s_mulk_i32 s43, 0x900
	s_ashr_i32 s47, s48, 31
	s_add_u32 s46, s48, s43
	s_addc_u32 s47, s47, 0
	s_mulk_i32 s7, 0x900
	s_ashr_i32 s43, s1, 31
	v_lshl_add_u64 v[176:177], s[46:47], 0, v[160:161]
	s_add_u32 s46, s7, s1
	s_addc_u32 s47, 0, s43
	v_lshl_add_u64 v[184:185], s[46:47], 0, v[160:161]
	v_lshlrev_b64 v[176:177], 11, v[176:177]
	v_lshlrev_b64 v[184:185], 11, v[184:185]
	v_lshl_add_u64 v[176:177], v[138:139], 0, v[176:177]
	v_lshl_add_u64 v[184:185], v[138:139], 0, v[184:185]
	global_load_dwordx2 v[178:179], v[176:177], off nt
	global_load_dwordx2 v[180:181], v[176:177], off offset:512 nt
	global_load_dwordx2 v[182:183], v[176:177], off offset:1024 nt
	s_cmp_eq_u64 vcc, 0
	global_load_dwordx2 v[176:177], v[176:177], off offset:1536 nt
	s_nop 0
	global_load_dwordx2 v[186:187], v[184:185], off nt
	global_load_dwordx2 v[188:189], v[184:185], off offset:512 nt
	global_load_dwordx2 v[190:191], v[184:185], off offset:1024 nt
	s_nop 0
	global_load_dwordx2 v[184:185], v[184:185], off offset:1536 nt
	s_waitcnt vmcnt(7)
	v_lshlrev_b32_e32 v198, 16, v178
	v_and_b32_e32 v199, 0xffff0000, v178
	s_waitcnt vmcnt(3)
	v_lshlrev_b32_e32 v206, 16, v186
	v_and_b32_e32 v207, 0xffff0000, v186
	v_lshlrev_b32_e32 v186, 16, v187
	v_and_b32_e32 v187, 0xffff0000, v187
	s_waitcnt vmcnt(2)
	v_lshlrev_b32_e32 v208, 16, v188
	v_and_b32_e32 v209, 0xffff0000, v188
	v_lshlrev_b32_e32 v188, 16, v189
	v_and_b32_e32 v189, 0xffff0000, v189
	s_waitcnt vmcnt(1)
	v_lshlrev_b32_e32 v210, 16, v190
	v_and_b32_e32 v211, 0xffff0000, v190
	v_lshlrev_b32_e32 v190, 16, v191
	v_and_b32_e32 v191, 0xffff0000, v191
	s_waitcnt vmcnt(0)
	v_lshlrev_b32_e32 v212, 16, v184
	v_and_b32_e32 v213, 0xffff0000, v184
	v_lshlrev_b32_e32 v184, 16, v185
	v_and_b32_e32 v185, 0xffff0000, v185
	v_lshlrev_b32_e32 v178, 16, v179
	v_and_b32_e32 v179, 0xffff0000, v179
	v_lshlrev_b32_e32 v200, 16, v180
	v_and_b32_e32 v201, 0xffff0000, v180
	v_lshlrev_b32_e32 v180, 16, v181
	v_and_b32_e32 v181, 0xffff0000, v181
	v_lshlrev_b32_e32 v202, 16, v182
	v_and_b32_e32 v203, 0xffff0000, v182
	v_lshlrev_b32_e32 v182, 16, v183
	v_and_b32_e32 v183, 0xffff0000, v183
	v_lshlrev_b32_e32 v204, 16, v176
	v_and_b32_e32 v205, 0xffff0000, v176
	v_lshlrev_b32_e32 v176, 16, v177
	v_and_b32_e32 v177, 0xffff0000, v177
	v_pk_mul_f32 v[184:185], s[6:7], v[184:185] op_sel_hi:[0,1]
	v_pk_mul_f32 v[212:213], s[6:7], v[212:213] op_sel_hi:[0,1]
	v_pk_mul_f32 v[190:191], s[6:7], v[190:191] op_sel_hi:[0,1]
	v_pk_mul_f32 v[210:211], s[6:7], v[210:211] op_sel_hi:[0,1]
	v_pk_mul_f32 v[188:189], s[6:7], v[188:189] op_sel_hi:[0,1]
	v_pk_mul_f32 v[208:209], s[6:7], v[208:209] op_sel_hi:[0,1]
	v_pk_mul_f32 v[186:187], s[6:7], v[186:187] op_sel_hi:[0,1]
	v_pk_mul_f32 v[206:207], s[6:7], v[206:207] op_sel_hi:[0,1]
	v_pk_fma_f32 v[198:199], s[0:1], v[198:199], v[206:207] op_sel_hi:[0,1,1]
	v_pk_fma_f32 v[178:179], s[0:1], v[178:179], v[186:187] op_sel_hi:[0,1,1]
	v_pk_fma_f32 v[186:187], s[0:1], v[200:201], v[208:209] op_sel_hi:[0,1,1]
	v_pk_fma_f32 v[180:181], s[0:1], v[180:181], v[188:189] op_sel_hi:[0,1,1]
	v_pk_fma_f32 v[188:189], s[0:1], v[202:203], v[210:211] op_sel_hi:[0,1,1]
	v_pk_fma_f32 v[182:183], s[0:1], v[182:183], v[190:191] op_sel_hi:[0,1,1]
	v_pk_fma_f32 v[190:191], s[0:1], v[204:205], v[212:213] op_sel_hi:[0,1,1]
	v_pk_fma_f32 v[176:177], s[0:1], v[176:177], v[184:185] op_sel_hi:[0,1,1]
	v_pk_add_f32 v[150:151], v[150:151], v[176:177]
	v_pk_add_f32 v[144:145], v[144:145], v[190:191]
	v_pk_add_f32 v[152:153], v[152:153], v[182:183]
	v_pk_add_f32 v[146:147], v[146:147], v[188:189]
	v_pk_add_f32 v[156:157], v[156:157], v[180:181]
	v_pk_add_f32 v[148:149], v[148:149], v[186:187]
	v_pk_add_f32 v[158:159], v[158:159], v[178:179]
	v_pk_add_f32 v[154:155], v[154:155], v[198:199]
	s_cbranch_scc1 .LBB0_137

.LBB0_1091:
	s_or_b64 exec, exec, s[34:35]
	s_mov_b64 s[0:1], -1
	s_and_b64 vcc, exec, s[58:59]
	s_waitcnt lgkmcnt(0)
	s_barrier
	s_cbranch_vccz .LBB0_1103
	v_readlane_b32 s0, v255, 32
	v_readlane_b32 s1, v255, 33
	v_readlane_b32 s4, v251, 35
	s_lshl_b64 s[0:1], s[0:1], 16
	v_readlane_b32 s18, v251, 49
	v_readlane_b32 s5, v251, 36
	v_readlane_b32 s6, v251, 37
	v_readlane_b32 s7, v251, 38
	v_readlane_b32 s8, v251, 39
	v_readlane_b32 s9, v251, 40
	v_readlane_b32 s10, v251, 41
	v_readlane_b32 s11, v251, 42
	v_readlane_b32 s12, v251, 43
	v_readlane_b32 s13, v251, 44
	v_readlane_b32 s14, v251, 45
	v_readlane_b32 s15, v251, 46
	v_readlane_b32 s16, v251, 47
	v_readlane_b32 s17, v251, 48
	v_readlane_b32 s19, v251, 50
	s_add_u32 s0, s18, s0
	s_addc_u32 s1, s19, s1
	v_readlane_b32 s4, v251, 1
	v_mov_b32_e32 v66, v0
	v_readlane_b32 s18, v251, 15
	v_readlane_b32 s2, v255, 28
	v_readlane_b32 s19, v251, 16
	v_ashrrev_i32_e32 v2, 6, v66
	v_readlane_b32 s3, v255, 29
	s_add_u32 s2, s18, s2
	v_and_b32_e32 v69, 63, v66
	v_add_u32_e32 v70, s89, v2
	s_addc_u32 s3, s19, s3
	v_lshlrev_b32_e32 v130, 4, v69
	v_lshlrev_b32_e32 v102, 3, v70
	global_load_dwordx4 v[2:5], v130, s[2:3]
	global_load_dwordx4 v[6:9], v130, s[2:3] offset:1024
	global_load_dwordx4 v[10:13], v130, s[2:3] offset:2048
	global_load_dwordx4 v[14:17], v130, s[2:3] offset:3072
	v_ashrrev_i32_e32 v103, 31, v102
	v_readlane_b32 s2, v251, 51
	v_lshlrev_b64 v[18:19], 12, v[102:103]
	v_readlane_b32 s3, v251, 52
	v_ashrrev_i32_e32 v67, 31, v66
	v_lshlrev_b64 v[34:35], 6, v[66:67]
	v_lshl_add_u64 v[18:19], s[2:3], 0, v[18:19]
	v_lshl_add_u64 v[18:19], v[18:19], 0, v[130:131]
	global_load_dwordx4 v[94:97], v[18:19], off nt
	global_load_dwordx4 v[90:93], v[18:19], off offset:1024 nt
	global_load_dwordx4 v[86:89], v[18:19], off offset:2048 nt
	global_load_dwordx4 v[82:85], v[18:19], off offset:3072 nt
	v_or_b32_e32 v18, 1, v102
	v_ashrrev_i32_e32 v19, 31, v18
	v_lshlrev_b64 v[18:19], 12, v[18:19]
	v_lshl_add_u64 v[18:19], s[2:3], 0, v[18:19]
	v_lshl_add_u64 v[30:31], v[18:19], 0, v[130:131]
	v_lshl_add_u64 v[50:51], s[0:1], 0, v[34:35]
	s_mov_b64 s[0:1], 0x8000
	global_load_dwordx4 v[18:21], v[30:31], off nt
	global_load_dwordx4 v[22:25], v[30:31], off offset:1024 nt
	global_load_dwordx4 v[26:29], v[30:31], off offset:2048 nt
	s_nop 0
	global_load_dwordx4 v[30:33], v[30:31], off offset:3072 nt
	s_nop 0
	global_load_dwordx4 v[34:37], v[50:51], off offset:48
	global_load_dwordx4 v[38:41], v[50:51], off offset:32
	global_load_dwordx4 v[42:45], v[50:51], off offset:16
	global_load_dwordx4 v[46:49], v[50:51], off
	v_lshl_add_u64 v[62:63], v[50:51], 0, s[0:1]
	v_add_co_u32_e32 v50, vcc, s77, v50
	v_readlane_b32 s14, v251, 11
	s_nop 0
	v_addc_co_u32_e32 v51, vcc, 0, v51, vcc
	global_load_dwordx4 v[50:53], v[50:51], off
	s_nop 0
	global_load_dwordx4 v[54:57], v[62:63], off offset:48
	global_load_dwordx4 v[58:61], v[62:63], off offset:32
	s_nop 0
	global_load_dwordx4 v[62:65], v[62:63], off offset:16
	v_readlane_b32 s5, v251, 2
	v_readlane_b32 s6, v251, 3
	v_readlane_b32 s7, v251, 4
	v_readlane_b32 s8, v251, 5
	v_readlane_b32 s9, v251, 6
	v_readlane_b32 s10, v251, 7
	v_readlane_b32 s11, v251, 8
	v_readlane_b32 s15, v251, 12
	v_lshlrev_b32_e32 v68, 2, v69
	s_mov_b32 s14, 0
	v_readlane_b32 s12, v251, 9
	v_readlane_b32 s13, v251, 10
	v_readlane_b32 s16, v251, 13
	v_readlane_b32 s17, v251, 14
	v_lshl_add_u32 v67, v66, 2, 0
	s_waitcnt vmcnt(0)
	ds_write2st64_b32 v67, v46, v50 offset1:8
	ds_write2st64_b32 v67, v47, v51 offset0:16 offset1:24
	ds_write2st64_b32 v67, v48, v52 offset0:32 offset1:40
	ds_write2st64_b32 v67, v49, v53 offset0:48 offset1:56
	ds_write2st64_b32 v67, v42, v62 offset0:64 offset1:72
	ds_write2st64_b32 v67, v43, v63 offset0:80 offset1:88
	ds_write2st64_b32 v67, v44, v64 offset0:96 offset1:104
	ds_write2st64_b32 v67, v45, v65 offset0:112 offset1:120
	ds_write2st64_b32 v67, v38, v58 offset0:128 offset1:136
	ds_write2st64_b32 v67, v39, v59 offset0:144 offset1:152
	ds_write2st64_b32 v67, v40, v60 offset0:160 offset1:168
	ds_write2st64_b32 v67, v41, v61 offset0:176 offset1:184
	ds_write2st64_b32 v67, v34, v54 offset0:192 offset1:200
	ds_write2st64_b32 v67, v35, v55 offset0:208 offset1:216
	ds_write2st64_b32 v67, v36, v56 offset0:224 offset1:232
	ds_write2st64_b32 v67, v37, v57 offset0:240 offset1:248
	v_and_b32_e32 v34, 8, v66
	v_lshl_add_u64 v[104:105], s[2:3], 0, v[130:131]
	v_cmp_eq_u32_e64 s[2:3], 0, v34
	v_and_b32_e32 v34, 4, v66
	v_cmp_eq_u32_e64 s[4:5], 0, v34
	v_and_b32_e32 v34, 16, v66
	v_cmp_eq_u32_e64 s[6:7], 0, v34
	v_and_b32_e32 v34, 3, v66
	v_cmp_eq_u32_e64 s[10:11], 0, v34
	v_lshlrev_b32_e32 v34, 3, v69
	v_sub_co_u32_e32 v36, vcc, 0, v34
	v_lshl_add_u64 v[106:107], s[92:93], 0, v[130:131]
	s_nop 0
	v_subb_co_u32_e64 v37, s[0:1], 0, 0, vcc
	v_lshl_add_u64 v[108:109], v[106:107], 0, v[36:37]
	v_lshl_add_u64 v[36:37], s[30:31], 0, v[130:131]
	s_mov_b64 s[0:1], 0x4835600
	v_lshl_add_u64 v[110:111], v[36:37], 0, s[0:1]
	v_readlane_b32 s0, v253, 13
	v_add_u32_e32 v128, 0, v130
	v_mov_b32_e32 v35, v131
	v_readlane_b32 s1, v253, 14
	v_and_b32_e32 v130, 60, v66
	v_add_u32_e32 v103, 0x4000, v70
	v_cmp_gt_u32_e64 s[8:9], 32, v69
	v_lshl_add_u64 v[112:113], s[0:1], 0, v[34:35]
	v_lshl_add_u64 v[114:115], s[90:91], 0, v[34:35]
	v_lshl_add_u64 v[116:117], s[96:97], 0, v[130:131]
	v_mov_b32_e32 v129, -1
	v_lshlrev_b32_e32 v130, 2, v68
	s_movk_i32 s15, 0x6000
	s_waitcnt lgkmcnt(0)
	s_barrier
	s_branch .LBB0_1094

.LBB0_1094:
	v_mov_b64_e32 v[36:37], v[32:33]
	v_mov_b64_e32 v[40:41], v[28:29]
	v_mov_b64_e32 v[44:45], v[24:25]
	v_mov_b64_e32 v[48:49], v[20:21]
	v_mov_b64_e32 v[34:35], v[30:31]
	v_mov_b64_e32 v[38:39], v[26:27]
	v_mov_b64_e32 v[42:43], v[22:23]
	v_mov_b64_e32 v[46:47], v[18:19]
	s_cmp_gt_u32 s14, 6
	v_add_u32_e32 v98, s14, v102
	s_cbranch_scc1 .LBB0_1096
	s_cmp_eq_u32 s14, 6
	v_add_u32_e32 v18, 2, v98
	s_cselect_b64 vcc, -1, 0
	v_cndmask_b32_e32 v18, v18, v103, vcc
	v_ashrrev_i32_e32 v19, 31, v18
	v_lshlrev_b64 v[18:19], 12, v[18:19]
	v_lshl_add_u64 v[30:31], v[104:105], 0, v[18:19]
	global_load_dwordx4 v[18:21], v[30:31], off nt
	global_load_dwordx4 v[22:25], v[30:31], off offset:1024 nt
	global_load_dwordx4 v[26:29], v[30:31], off offset:2048 nt
	s_nop 0
	global_load_dwordx4 v[30:33], v[30:31], off offset:3072 nt
